# v40 + first grid barrier's WAIT moved behind P1's pooling of x (and the pre-half's weight pre-tiling): only the first read of the pre-tiled pool weights needs it
# speedup vs baseline: 1.0051x; 1.0051x over previous
.LBB0_43:
	s_or_b64 exec, exec, s[2:3]
	s_getreg_b32 s2, hwreg(HW_REG_XCC_ID, 0, 4)
	s_waitcnt lgkmcnt(0)
	v_readlane_b32 s2, v254, 0
	s_and_b32 s2, s2, 8
	s_cmp_eq_u32 s2, 0
	s_cselect_b64 s[26:27], -1, 0
	s_cmp_lg_u32 s2, 0
	s_cselect_b64 s[2:3], -1, 0
	v_writelane_b32 v254, s2, 5
	s_and_b64 vcc, exec, s[26:27]
	s_nop 0
	v_writelane_b32 v254, s3, 6
	s_cbranch_vccnz .LBB0_85
	s_and_saveexec_b64 s[4:5], s[24:25]
	s_cbranch_execz .LBB0_62
	s_load_dwordx2 s[2:3], s[0:1], 0x48
	s_load_dwordx2 s[6:7], s[0:1], 0xa8
	s_mov_b64 s[10:11], 0x80000
	s_mov_b64 s[12:13], 0
	v_mov_b32_e32 v5, 0
	s_waitcnt lgkmcnt(0)
	s_add_u32 s8, s2, 0x100000
	v_lshl_add_u64 v[2:3], v[210:211], 4, s[6:7]
	s_addc_u32 s9, s3, 0
	s_ashr_i32 s21, s20, 31
	v_lshl_add_u64 v[2:3], v[2:3], 0, s[10:11]
	s_lshl_b64 s[10:11], s[20:21], 4
	s_movk_i32 s2, 0x1000
	s_movk_i32 s3, 0x7fff
	v_mov_b32_e32 v1, v210

.LBB0_118:
	v_add_u32_e32 v2, 64, v3
	v_cvt_f32_i32_e32 v2, v2
	s_bfe_u32 s10, s29, 0x10006
	s_lshl_b32 s11, s65, 5
	v_and_b32_e32 v214, 63, v221
	v_readlane_b32 s4, v254, 55
	s_nop 1
	v_add3_u32 v9, s4, v69, v68
	s_lshl_b32 s4, s65, 16
	s_lshl_b32 s5, s10, 15
	s_or_b32 s4, s5, s4
	s_ashr_i32 s5, s4, 31
	s_lshl_b64 s[4:5], s[4:5], 1
	v_rcp_f32_e32 v2, v2
	s_nop 0
	s_waitcnt lgkmcnt(0)
	s_add_u32 s8, s16, s4
	v_pk_fma_f32 v[2:3], v[6:7], v[2:3], v[4:5] op_sel_hi:[1,0,1] neg_lo:[0,0,1] neg_hi:[0,0,1]
	s_addc_u32 s9, s17, s5
	v_lshlrev_b32_e32 v212, 4, v214
	v_cvt_pk_bf16_f32 v2, v2, v3
	v_lshl_add_u64 v[146:147], s[8:9], 0, v[212:213]
	s_mov_b32 s29, s23
	ds_write_b32 v9, v2
	v_lshl_add_u64 v[2:3], v[146:147], 0, s[28:29]
	s_mov_b32 s31, s23
	s_mov_b32 s35, s23
	s_waitcnt lgkmcnt(0)
	s_barrier
	s_mov_b64 s[98:99], exec
	v_readlane_b32 s4, v254, 1
	v_readlane_b32 s5, v254, 2
	s_and_b64 s[4:5], s[98:99], s[4:5]
	s_mov_b64 exec, s[4:5]
	s_cbranch_execz .Lmy_gw_end
	s_load_dwordx2 s[100:101], s[0:1], 0x80
	v_mov_b32_e32 v245, 0x22ff8
	ds_read_b32 v245, v245
	v_mov_b32_e32 v246, 0
	s_mov_b32 s12, 0
	s_waitcnt lgkmcnt(0)
	s_add_u32 s14, s100, 0x3500
	s_addc_u32 s15, s101, 0
	v_add_u32_e32 v245, 1, v245
.Lmy_gw_poll:
	global_load_dword v247, v246, s[14:15] sc1
	s_waitcnt vmcnt(0)
	v_sub_u32_e32 v247, v247, v245
	v_cmp_gt_i32_e32 vcc, 0, v247
	s_cbranch_vccz .Lmy_gw_done
	s_sleep 1
	s_add_i32 s12, s12, 1
	s_and_b32 s13, s12, 0xff
	s_cmp_lg_u32 s13, 0
	s_cbranch_scc1 .Lmy_gw_poll
	global_load_dword v247, v246, s[100:101] offset:512 sc1
	s_waitcnt vmcnt(0)
	v_cmp_ne_u32_e32 vcc, 0, v247
	s_cbranch_vccnz .Lmy_gw_done
	s_cmp_le_u32 s12, 0x40000
	s_cbranch_scc1 .Lmy_gw_poll
	v_mov_b32_e32 v247, 1
	global_atomic_add v246, v247, s[100:101] offset:512

.Lmy_gw_end:
	s_mov_b64 exec, s[98:99]
	s_barrier
	v_lshl_add_u64 v[4:5], v[146:147], 0, s[30:31]
	global_load_dwordx4 v[70:73], v[2:3], off
	global_load_dwordx4 v[74:77], v[4:5], off
	v_lshl_add_u64 v[2:3], v[146:147], 0, s[34:35]
	s_mov_b32 s39, s23
	s_mov_b32 s41, s23
	v_lshl_add_u64 v[4:5], v[146:147], 0, s[38:39]
	global_load_dwordx4 v[78:81], v[2:3], off
	global_load_dwordx4 v[66:69], v[4:5], off
	v_lshl_add_u64 v[2:3], v[146:147], 0, s[40:41]
	s_mov_b32 s43, s23
	s_mov_b32 s45, s23
	v_lshl_add_u64 v[4:5], v[146:147], 0, s[42:43]
	global_load_dwordx4 v[82:85], v[2:3], off
	global_load_dwordx4 v[86:89], v[4:5], off
	v_lshl_add_u64 v[2:3], v[146:147], 0, s[44:45]
	s_mov_b32 s47, s23
	s_mov_b32 s49, s23
	v_lshl_add_u64 v[4:5], v[146:147], 0, s[46:47]
	global_load_dwordx4 v[94:97], v[2:3], off
	global_load_dwordx4 v[90:93], v[4:5], off
	v_lshl_add_u64 v[2:3], v[146:147], 0, s[48:49]
	s_mov_b32 s51, s23
	s_mov_b32 s53, s23
	v_lshl_add_u64 v[4:5], v[146:147], 0, s[50:51]
	global_load_dwordx4 v[98:101], v[2:3], off
	global_load_dwordx4 v[102:105], v[4:5], off
	v_lshl_add_u64 v[2:3], v[146:147], 0, s[52:53]
	s_mov_b32 s55, s23
	s_mov_b32 s57, s23
	v_lshl_add_u64 v[4:5], v[146:147], 0, s[54:55]
	global_load_dwordx4 v[110:113], v[2:3], off
	global_load_dwordx4 v[106:109], v[4:5], off
	v_lshl_add_u64 v[2:3], v[146:147], 0, s[56:57]
	s_mov_b32 s59, s23
	s_mov_b32 s61, s23
	v_lshl_add_u64 v[4:5], v[146:147], 0, s[58:59]
	global_load_dwordx4 v[114:117], v[2:3], off
	global_load_dwordx4 v[118:121], v[4:5], off
	v_lshl_add_u64 v[2:3], v[146:147], 0, s[60:61]
	s_mov_b32 s63, s23
	v_lshl_add_u64 v[4:5], v[146:147], 0, s[62:63]
	global_load_dwordx4 v[126:129], v[2:3], off
	global_load_dwordx4 v[122:125], v[4:5], off
	v_readlane_b32 s4, v254, 13
	v_and_b32_e32 v222, 15, v221
	v_bfe_u32 v2, v221, 4, 2
	s_or_b32 s4, s11, s4
	v_lshl_add_u32 v223, v222, 11, 0
	v_bitop3_b32 v3, s4, v222, v2 bitop3:0x36
	v_lshl_add_u32 v148, v3, 4, v223
	v_add_u32_e32 v149, 0x10000, v148
	ds_read_b128 v[130:133], v148
	ds_read_b128 v[134:137], v148 offset:32768
	v_add_u32_e32 v150, 0x18000, v148
	ds_read_b128 v[142:145], v149
	ds_read_b128 v[138:141], v150
	v_or_b32_e32 v224, s11, v2
	v_mov_b32_e32 v2, 0
	s_mov_b32 s11, 0
	s_mov_b64 s[4:5], -1
	v_mov_b32_e32 v3, v2
	v_mov_b32_e32 v4, v2
	v_mov_b32_e32 v5, v2
	v_mov_b32_e32 v6, v2
	v_mov_b32_e32 v7, v2
	v_mov_b32_e32 v8, v2
	v_mov_b32_e32 v9, v2
	v_mov_b32_e32 v10, v2
	v_mov_b32_e32 v11, v2
	v_mov_b32_e32 v12, v2
	v_mov_b32_e32 v13, v2
	v_mov_b32_e32 v14, v2
	v_mov_b32_e32 v15, v2
	v_mov_b32_e32 v16, v2
	v_mov_b32_e32 v17, v2
	v_mov_b32_e32 v18, v2
	v_mov_b32_e32 v19, v2
	v_mov_b32_e32 v20, v2
	v_mov_b32_e32 v21, v2
	v_mov_b32_e32 v22, v2
	v_mov_b32_e32 v23, v2
	v_mov_b32_e32 v24, v2
	v_mov_b32_e32 v25, v2
	v_mov_b32_e32 v26, v2
	v_mov_b32_e32 v27, v2
	v_mov_b32_e32 v28, v2
	v_mov_b32_e32 v29, v2
	v_mov_b32_e32 v30, v2
	v_mov_b32_e32 v31, v2
	v_mov_b32_e32 v32, v2
	v_mov_b32_e32 v33, v2
	v_mov_b32_e32 v34, v2
	v_mov_b32_e32 v35, v2
	v_mov_b32_e32 v36, v2
	v_mov_b32_e32 v37, v2
	v_mov_b32_e32 v38, v2
	v_mov_b32_e32 v39, v2
	v_mov_b32_e32 v40, v2
	v_mov_b32_e32 v41, v2
	v_mov_b32_e32 v42, v2
	v_mov_b32_e32 v43, v2
	v_mov_b32_e32 v44, v2
	v_mov_b32_e32 v45, v2
	v_mov_b32_e32 v46, v2
	v_mov_b32_e32 v47, v2
	v_mov_b32_e32 v48, v2
	v_mov_b32_e32 v49, v2
	v_mov_b32_e32 v50, v2
	v_mov_b32_e32 v51, v2
	v_mov_b32_e32 v52, v2
	v_mov_b32_e32 v53, v2
	v_mov_b32_e32 v54, v2
	v_mov_b32_e32 v55, v2
	v_mov_b32_e32 v56, v2
	v_mov_b32_e32 v57, v2
	v_mov_b32_e32 v58, v2
	v_mov_b32_e32 v59, v2
	v_mov_b32_e32 v60, v2
	v_mov_b32_e32 v61, v2
	v_mov_b32_e32 v62, v2
	v_mov_b32_e32 v63, v2
	v_mov_b32_e32 v64, v2
	v_mov_b32_e32 v65, v2
